# exact vmcnt counts at tile boundaries in the in-proj and MoE-down K-loops: prefetch loads in the last iteration and epilogue stores before the first iteration are counted instead of waited for
# baseline (speedup 1.0000x reference)
; __device__ __forceinline__ void p0_transpose_item_bf16(const float* W, int ldw, int k0, int n0, bf16_t* WT, int K, int drow0, const float* sc, LAS unsigned char* tile, int lane) {
;     const int kq = lane >> 4, nq = lane & 15;
;     const float* src = W + (size_t)(k0 + 4 * kq) * ldw + n0 + 4 * nq;
; #pragma unroll
;     for (int hb = 0; hb < 2; ++hb) {
;         f32x4 v[4][4], sv[4];
;         const float* scp = sc ? sc + k0 + 64 * hb + 4 * kq : src;
; #pragma unroll
;         for (int i = 0; i < 4; ++i) sv[i] = *(const f32x4*)(scp + (sc ? 16 * i : 0));
; #pragma unroll
;         for (int i = 0; i < 4; ++i)
; #pragma unroll
;             for (int j = 0; j < 4; ++j) v[i][j] = *(const f32x4*)(src + (size_t)(64 * hb + 16 * i + j) * ldw);
; #pragma unroll
;         for (int i = 0; i < 4; ++i) {
;             const f32x4 s4 = sc ? sv[i] : (f32x4){1.f, 1.f, 1.f, 1.f};
; #pragma unroll
;             for (int nn = 0; nn < 4; ++nn) { u32x2 t; t.x = cvt_pk_bf16(v[i][0][nn] * s4[0], v[i][1][nn] * s4[1]); t.y = cvt_pk_bf16(v[i][2][nn] * s4[2], v[i][3][nn] * s4[3]);
;                 const int chunk = 2 * (4 * hb + i) + (kq >> 1);
;                 *(LAS u32x2*)(tile + (4 * nq + nn) * 256 + ((chunk ^ nq) << 4) + ((kq & 1) << 3)) = t; }
;         }
;     }
;     asm volatile("s_waitcnt lgkmcnt(0)" ::: "memory");
; #pragma unroll
;     for (int r = 0; r < 16; ++r) { const int n = (lane >> 4) + 4 * r, c = lane & 15;
;         const u32x4 o = *(const LAS u32x4*)(tile + n * 256 + ((c ^ ((n >> 2) & 15)) << 4));
; __global__ void __launch_bounds__(512, 2) hymba_fwd(Params p) {
;     ...
;     if (IN(1)) {
;         const int ng = (F.G == 256) ? NG_GEMM : F.G;
;         if ((int)blockIdx.x < ng) {
;             pg8::Gemm g{(const bf16_t*)(ws + WS_XB), (const bf16_t*)(ws + WS_WIN), DM}; pg8::StaticOrder S; S.init(T_TOK, NPROJ, ng, (int)blockIdx.x);
;             EpiProj E{(bf16_t*)(ws + WS_PROJ), (const float*)(ws + WS_RSTD1)};
;             pg8::gemm_phase<EpiProj, pg8::StaticOrder, false, false, true, false>(ring, g, S, E);
;             if (ng == F.G) { wout_transpose(p, F, (int)blockIdx.x * 8 + F.wave, F.G * 8); moe_weight_convert(p, F, (int)blockIdx.x * 8 + F.wave, F.G * 8, 0, CONV_N_GU); }
;         } else { wout_transpose(p, F, ((int)blockIdx.x - ng) * 8 + F.wave, (F.G - ng) * 8); moe_weight_convert(p, F, ((int)blockIdx.x - ng) * 8 + F.wave, (F.G - ng) * 8, 0, CONV_N_GU); }
.LBB0_145:
	s_mov_b32 s99, 0
	v_readlane_b32 s4, v245, 4
	s_cmp_lt_i32 s4, 2
	s_cselect_b64 s[0:1], -1, 0
	s_and_b64 s[2:3], s[0:1], s[2:3]
	s_andn2_b64 vcc, exec, s[2:3]
	v_readlane_b32 s5, v245, 5
	v_readlane_b32 s6, v245, 6
	v_readlane_b32 s7, v245, 7
	s_cbranch_vccnz .LBB0_233
	s_cmpk_lg_i32 s94, 0x100
	s_cselect_b64 s[12:13], -1, 0
	s_and_b64 s[2:3], s[12:13], exec
	s_cselect_b32 s20, s94, 0xb4
	v_readlane_b32 s2, v245, 18
	s_cmp_ge_i32 s2, s20
	s_mov_b64 s[2:3], -1
	s_cbranch_scc0 .LBB0_182
	v_readlane_b32 s2, v245, 18
	s_sub_i32 s2, s2, s20
	s_lshl_b32 s6, s2, 3
	s_sub_i32 s2, s94, s20
	s_add_i32 s6, s6, s54
	s_lshl_b32 s21, s2, 3
	v_readlane_b32 s56, v245, 39
	s_cmpk_gt_u32 s6, 0x1ff
	v_readlane_b32 s60, v245, 43
	v_readlane_b32 s61, v245, 44
	v_readlane_b32 s62, v245, 45
	v_readlane_b32 s63, v245, 46
	s_barrier
	v_readlane_b32 s57, v245, 40
	v_readlane_b32 s58, v245, 41
	v_readlane_b32 s59, v245, 42
	v_readlane_b32 s64, v245, 47
	v_readlane_b32 s65, v245, 48
	v_readlane_b32 s66, v245, 49
	v_readlane_b32 s67, v245, 50
	v_readlane_b32 s68, v245, 51
	v_readlane_b32 s69, v245, 52
	v_readlane_b32 s70, v245, 53
	v_readlane_b32 s71, v245, 54
	s_cbranch_scc1 .LBB0_150
	s_lshl_b32 s2, s54, 14
	v_lshrrev_b32_e32 v5, 1, v162
	s_add_i32 s4, s2, 0
	v_and_b32_e32 v2, 15, v0
	v_lshrrev_b32_e32 v4, 5, v162
	v_and_b32_e32 v5, 8, v5
	v_lshrrev_b32_e32 v1, 4, v162
	v_lshlrev_b32_e32 v8, 2, v2
	v_mov_b32_e32 v3, 0
	v_add_u32_e32 v5, s4, v5
	v_bitop3_b32 v7, v4, v0, 15 bitop3:0x78
	v_lshlrev_b32_e32 v9, 10, v2
	v_bitop3_b32 v10, v4, v2, 2 bitop3:0x36
	v_bitop3_b32 v11, v4, v2, 4 bitop3:0x36
	v_bitop3_b32 v12, v4, v2, 6 bitop3:0x36
	v_bitop3_b32 v13, v4, v2, 8 bitop3:0x36
	v_bitop3_b32 v14, v4, v2, 10 bitop3:0x36
	v_bitop3_b32 v15, v4, v2, 12 bitop3:0x36
	v_bitop3_b32 v4, v4, v2, 14 bitop3:0x36
	v_lshlrev_b32_e32 v2, 4, v2
	v_lshl_add_u32 v7, v7, 4, v5
	v_lshl_add_u32 v10, v10, 4, v5
	v_lshl_add_u32 v11, v11, 4, v5
	v_lshl_add_u32 v12, v12, 4, v5
	v_lshl_add_u32 v13, v13, 4, v5
	v_lshl_add_u32 v14, v14, 4, v5
	v_lshl_add_u32 v15, v15, 4, v5
	v_lshl_add_u32 v16, v4, 4, v5
	v_lshl_add_u64 v[4:5], s[96:97], 0, v[2:3]
	v_lshl_add_u32 v17, v1, 8, s4
	v_lshlrev_b32_e32 v2, 4, v0
	v_mov_b32_e32 v20, 0xf0
	s_movk_i32 s4, 0x80
	v_bitop3_b32 v35, v2, s4, v20 bitop3:0x6c
	s_movk_i32 s4, 0x90
	v_bitop3_b32 v37, v2, s4, v20 bitop3:0x6c
	s_movk_i32 s4, 0xa0
	s_mov_b64 s[2:3], 0x31000000
	v_bitop3_b32 v39, v2, s4, v20 bitop3:0x6c
	s_movk_i32 s4, 0xb0
	v_lshl_add_u64 v[4:5], v[4:5], 0, s[2:3]
	s_movk_i32 s2, 0x50
	v_bitop3_b32 v41, v2, s4, v20 bitop3:0x6c
	s_movk_i32 s4, 0xc0
	v_bitop3_b32 v29, v2, s2, v20 bitop3:0x6c
	s_movk_i32 s2, 0x60
	v_bitop3_b32 v43, v2, s4, v20 bitop3:0x6c
	s_movk_i32 s4, 0xd0
	s_movk_i32 s3, 0xf0
	v_bitop3_b32 v31, v2, s2, v20 bitop3:0x6c
	s_movk_i32 s2, 0x70
	v_bitop3_b32 v45, v2, s4, v20 bitop3:0x6c
	s_movk_i32 s4, 0xe0
	v_and_b32_e32 v18, 0xf0, v2
	v_add_u32_e32 v19, 0x400, v17
	v_bitop3_b32 v21, v2, 16, v20 bitop3:0x6c
	v_add_u32_e32 v22, 0x800, v17
	v_bitop3_b32 v23, v2, 32, v20 bitop3:0x6c
	v_add_u32_e32 v24, 0xc00, v17
	v_bitop3_b32 v25, v2, 48, v20 bitop3:0x6c
	v_add_u32_e32 v26, 0x1000, v17
	v_bitop3_b32 v27, v2, 64, v20 bitop3:0x6c
	v_add_u32_e32 v28, 0x1400, v17
	v_add_u32_e32 v30, 0x1800, v17
	v_add_u32_e32 v32, 0x1c00, v17
	v_bitop3_b32 v33, v2, s2, v20 bitop3:0x6c
	v_add_u32_e32 v34, 0x2000, v17
	v_add_u32_e32 v36, 0x2400, v17
	v_add_u32_e32 v38, 0x2800, v17
	v_add_u32_e32 v40, 0x2c00, v17
	v_add_u32_e32 v42, 0x3000, v17
	v_add_u32_e32 v44, 0x3400, v17
	v_add_u32_e32 v46, 0x3800, v17
	v_bitop3_b32 v47, v2, s4, v20 bitop3:0x6c
	v_add_u32_e32 v48, 0x3c00, v17
	v_bitop3_b32 v49, v2, s3, v2 bitop3:0xc
	v_add_u32_e32 v50, v7, v9
	v_add_u32_e32 v51, v10, v9
	v_add_u32_e32 v52, v11, v9
	v_add_u32_e32 v53, v12, v9
	v_add_u32_e32 v54, v13, v9
	v_add_u32_e32 v55, v14, v9
	v_add_u32_e32 v56, v15, v9
	v_add_u32_e32 v57, v16, v9
	v_lshlrev_b32_e32 v6, 2, v1
	s_movk_i32 s2, 0x2000
	s_lshl_b32 s3, s6, 6
	s_lshl_b32 s4, s21, 6
	v_lshlrev_b32_e32 v2, 2, v8
	s_movk_i32 s5, 0x4000
	s_movk_i32 s7, 0x6000
	s_mov_b32 s8, 0x20000
	s_mov_b32 s9, 0x22000
	s_mov_b32 s10, 0x24000
	s_mov_b32 s11, 0x26000
	s_mov_b32 s14, 0x40000
	s_mov_b32 s15, 0x42000
	s_mov_b32 s16, 0x44000
	s_mov_b32 s17, 0x46000
	s_mov_b32 s18, 0x60000
	s_mov_b32 s19, 0x62000
	s_mov_b32 s22, 0x64000
	s_mov_b32 s23, 0x66000
	s_mov_b32 s24, 0x80000
	s_mov_b32 s25, 0x82000
	s_mov_b32 s26, 0x84000
	s_mov_b32 s27, 0x86000
	s_mov_b32 s28, 0xa0000
	s_mov_b32 s29, 0xa2000
	s_mov_b32 s30, 0xa4000
	s_mov_b32 s31, 0xa6000
	s_mov_b32 s33, 0xc0000
	s_mov_b32 s34, 0xc2000
	s_mov_b32 s35, 0xc4000
	s_mov_b32 s36, 0xc6000
	s_mov_b32 s37, 0xe0000
	s_mov_b32 s38, 0xe2000
	s_mov_b32 s39, 0xe4000
	s_mov_b32 s40, 0xe6000
	v_add_u32_e32 v7, v17, v18
	v_add_u32_e32 v8, v19, v21
	v_add_u32_e32 v9, v22, v23
	v_add_u32_e32 v10, v24, v25
	v_add_u32_e32 v11, v26, v27
	v_add_u32_e32 v12, v28, v29
	v_add_u32_e32 v13, v30, v31
	v_add_u32_e32 v14, v32, v33
	v_add_u32_e32 v15, v34, v35
	v_add_u32_e32 v16, v36, v37
	v_add_u32_e32 v17, v38, v39
	v_add_u32_e32 v18, v40, v41
	v_add_u32_e32 v19, v42, v43
	v_add_u32_e32 v20, v44, v45
	v_add_u32_e32 v21, v46, v47
	v_add_u32_e32 v22, v48, v49
	v_add_u32_e32 v23, 0x4000, v50
	v_add_u32_e32 v24, 0x4000, v51
	v_add_u32_e32 v25, 0x4000, v52
	v_add_u32_e32 v26, 0x4000, v53
	v_add_u32_e32 v27, 0x4000, v54
	v_add_u32_e32 v28, 0x4000, v55
	v_add_u32_e32 v29, 0x4000, v56
	v_add_u32_e32 v30, 0x4000, v57
	s_mov_b32 s41, s6

; template <class Epi, class Sched, bool GATHER, bool ALIGN_EPI, bool SP2, bool FP8>
; __device__ __forceinline__ void gemm_phase(LAS unsigned char* lds, const Gemm g, const Sched& S, const Epi& E) {
;     ...
;             asm volatile("s_nop 15\n\ts_nop 3" : "+v"(acc[0][0][0][0]), "+v"(acc[0][0][0][1]), "+v"(acc[0][0][1][0]), "+v"(acc[0][0][1][1]), "+v"(acc[0][0][2][0]), "+v"(acc[0][0][2][1]), "+v"(acc[0][0][3][0]), "+v"(acc[0][0][3][1]));
;             asm volatile("" : "+v"(acc[0][1][0][0]), "+v"(acc[0][1][0][1]), "+v"(acc[0][1][1][0]), "+v"(acc[0][1][1][1]), "+v"(acc[0][1][2][0]), "+v"(acc[0][1][2][1]), "+v"(acc[0][1][3][0]), "+v"(acc[0][1][3][1]));
;             asm volatile("" : "+v"(acc[1][0][0][0]), "+v"(acc[1][0][0][1]), "+v"(acc[1][0][1][0]), "+v"(acc[1][0][1][1]), "+v"(acc[1][0][2][0]), "+v"(acc[1][0][2][1]), "+v"(acc[1][0][3][0]), "+v"(acc[1][0][3][1]));
;             asm volatile("" : "+v"(acc[1][1][0][0]), "+v"(acc[1][1][0][1]), "+v"(acc[1][1][1][0]), "+v"(acc[1][1][1][1]), "+v"(acc[1][1][2][0]), "+v"(acc[1][1][2][1]), "+v"(acc[1][1][3][0]), "+v"(acc[1][1][3][1]));
;         }
;         { Unit eu = cur; asm volatile("" : "+s"(eu.pm), "+s"(eu.pn), "+s"(eu.e), "+s"(eu.r0));
;           int tid2 = threadIdx.x; asm volatile("" : "+v"(tid2));
;           const int wid2 = __builtin_amdgcn_readfirstlane(tid2 >> 6), lane2 = tid2 & 63;
;           E(acc, eu, pre, wid2 >> 2, wid2 & 3, lane2 & 15, lane2 >> 4); }
;     __device__ __forceinline__ void operator()(const f32x4 (&acc)[2][2][4][2], const pg8::Unit& u, const Pre& pre, int wr, int wc, int fr, int fq) const {
;         const int row0 = u.pm * 256 + wr * 64 + fr, col0 = u.pn * 256 + wc * 32 + 8 * fq;
;         float rsv[8];
; #pragma unroll
;         for (int i = 0; i < 4; ++i) { rsv[i] = pre.ra[i]; rsv[4 + i] = pre.rb[i]; }
; #pragma unroll
;         for (int ai = 0; ai < 2; ++ai)
; #pragma unroll
;             for (int m = 0; m < 4; ++m) { const int row = row0 + ai * 128 + m * 16; const float rs = rsv[ai * 4 + m]; bf16_t* rowp = O + (size_t)row * NPROJ + col0;
; #pragma unroll
;                 for (int bj = 0; bj < 2; ++bj) { const f32x4 v0 = acc[ai][bj][m][0] * rs, v1 = acc[ai][bj][m][1] * rs;
;                     u32x4 w; w.x = cvt_pk_bf16(v0[0], v0[1]); w.y = cvt_pk_bf16(v0[2], v0[3]); w.z = cvt_pk_bf16(v1[0], v1[1]); w.w = cvt_pk_bf16(v1[2], v1[3]);
.LBB0_187:
	s_mov_b32 s99, 1
	s_mov_b32 s10, 0
	s_mov_b32 s11, 0
	s_nop 15
	s_nop 3
	v_mov_b32_e32 v130, v0
	s_lshl_b32 s11, s47, 8
	v_readfirstlane_b32 s10, v130
	s_ashr_i32 s47, s10, 2
	s_andn2_b32 s47, s47, 63
	s_lshr_b32 s10, s10, 1
	s_add_i32 s47, s47, s11
	s_and_b32 s10, s10, 0x60
	s_lshl_b32 s11, s46, 8
	v_and_or_b32 v138, v130, 15, s47
	v_lshrrev_b32_e32 v130, 1, v130
	s_or_b32 s10, s10, s11
	v_and_or_b32 v132, v130, 24, s10
	v_ashrrev_i32_e32 v133, 31, v132
	v_mov_b64_e32 v[130:131], s[14:15]
	v_mad_i64_i32 v[134:135], s[10:11], v138, s42, v[130:131]
	v_lshlrev_b64 v[132:133], 1, v[132:133]
	s_waitcnt vmcnt(21)
	v_pk_mul_f32 v[128:129], v[172:173], v[128:129] op_sel_hi:[0,1]
	v_pk_mul_f32 v[126:127], v[172:173], v[126:127] op_sel_hi:[0,1]
	v_pk_mul_f32 v[136:137], v[172:173], v[124:125] op_sel_hi:[0,1]
	v_pk_mul_f32 v[124:125], v[172:173], v[122:123] op_sel_hi:[0,1]
	v_lshl_add_u64 v[134:135], v[134:135], 0, v[132:133]
	v_cvt_pk_bf16_f32 v122, v126, v127
	v_cvt_pk_bf16_f32 v123, v128, v129
	v_cvt_pk_bf16_f32 v124, v124, v125
	v_cvt_pk_bf16_f32 v125, v136, v137
	global_store_dwordx4 v[134:135], v[122:125], off
	v_pk_mul_f32 v[116:117], v[172:173], v[116:117] op_sel_hi:[0,1]
	v_pk_mul_f32 v[114:115], v[172:173], v[114:115] op_sel_hi:[0,1]
	v_pk_mul_f32 v[122:123], v[172:173], v[108:109] op_sel_hi:[0,1]
	v_pk_mul_f32 v[108:109], v[172:173], v[106:107] op_sel_hi:[0,1]
	v_cvt_pk_bf16_f32 v106, v114, v115
	v_cvt_pk_bf16_f32 v107, v116, v117
	v_cvt_pk_bf16_f32 v108, v108, v109
	v_cvt_pk_bf16_f32 v109, v122, v123
	global_store_dwordx4 v[134:135], v[106:109], off offset:256
	v_pk_mul_f32 v[112:113], v[172:173], v[112:113] op_sel:[1,0]
	v_pk_mul_f32 v[110:111], v[172:173], v[110:111] op_sel:[1,0]
	v_or_b32_e32 v106, 16, v138
	v_mad_i64_i32 v[106:107], s[10:11], v106, s42, v[130:131]
	v_lshl_add_u64 v[114:115], v[106:107], 0, v[132:133]
	v_pk_mul_f32 v[108:109], v[172:173], v[120:121] op_sel:[1,0]
	v_pk_mul_f32 v[106:107], v[172:173], v[118:119] op_sel:[1,0]
	v_pk_mul_f32 v[100:101], v[172:173], v[100:101] op_sel:[1,0]
	v_cvt_pk_bf16_f32 v106, v106, v107
	v_cvt_pk_bf16_f32 v107, v108, v109
	v_cvt_pk_bf16_f32 v108, v110, v111
	v_cvt_pk_bf16_f32 v109, v112, v113
	global_store_dwordx4 v[114:115], v[106:109], off
	v_pk_mul_f32 v[98:99], v[172:173], v[98:99] op_sel:[1,0]
	s_waitcnt vmcnt(19)
; __device__ __forceinline__ unsigned cvt_pk_bf16(float lo, float hi) { const f32x2_t v = {lo, hi}; return __builtin_bit_cast(unsigned, __builtin_convertvector(v, bf16x2_t)); }
;     __device__ __forceinline__ void operator()(const f32x4 (&acc)[2][2][4][2], const pg8::Unit& u, const Pre& pre, int wr, int wc, int fr, int fq) const {
;     ...
;             for (int m = 0; m < 4; ++m) { const int row = row0 + ai * 128 + m * 16; const float rs = rsv[ai * 4 + m]; bf16_t* rowp = O + (size_t)row * NPROJ + col0;
; #pragma unroll
;                 for (int bj = 0; bj < 2; ++bj) { const f32x4 v0 = acc[ai][bj][m][0] * rs, v1 = acc[ai][bj][m][1] * rs;
;                     u32x4 w; w.x = cvt_pk_bf16(v0[0], v0[1]); w.y = cvt_pk_bf16(v0[2], v0[3]); w.z = cvt_pk_bf16(v1[0], v1[1]); w.w = cvt_pk_bf16(v1[2], v1[3]);
;                     *(u32x4*)(rowp + bj * 128) = w; } }
	v_pk_mul_f32 v[96:97], v[176:177], v[96:97] op_sel_hi:[0,1]
	v_pk_mul_f32 v[106:107], v[172:173], v[92:93] op_sel:[1,0]
	v_pk_mul_f32 v[92:93], v[172:173], v[90:91] op_sel:[1,0]
	v_cvt_pk_bf16_f32 v90, v98, v99
	v_cvt_pk_bf16_f32 v91, v100, v101
	v_cvt_pk_bf16_f32 v92, v92, v93
	v_cvt_pk_bf16_f32 v93, v106, v107
	global_store_dwordx4 v[114:115], v[90:93], off offset:256
	v_pk_mul_f32 v[94:95], v[176:177], v[94:95] op_sel_hi:[0,1]
	v_pk_mul_f32 v[84:85], v[176:177], v[84:85] op_sel_hi:[0,1]
	v_or_b32_e32 v90, 32, v138
	v_mad_i64_i32 v[90:91], s[10:11], v90, s42, v[130:131]
	v_lshl_add_u64 v[98:99], v[90:91], 0, v[132:133]
	v_pk_mul_f32 v[92:93], v[176:177], v[104:105] op_sel_hi:[0,1]
	v_pk_mul_f32 v[90:91], v[176:177], v[102:103] op_sel_hi:[0,1]
	v_cvt_pk_bf16_f32 v90, v90, v91
	v_cvt_pk_bf16_f32 v91, v92, v93
	v_cvt_pk_bf16_f32 v92, v94, v95
	v_cvt_pk_bf16_f32 v93, v96, v97
	global_store_dwordx4 v[98:99], v[90:93], off
	v_pk_mul_f32 v[82:83], v[176:177], v[82:83] op_sel_hi:[0,1]
	v_pk_mul_f32 v[64:65], v[170:171], v[64:65] op_sel_hi:[0,1]
	v_pk_mul_f32 v[90:91], v[176:177], v[76:77] op_sel_hi:[0,1]
	v_pk_mul_f32 v[76:77], v[176:177], v[74:75] op_sel_hi:[0,1]
	v_cvt_pk_bf16_f32 v74, v82, v83
	v_cvt_pk_bf16_f32 v75, v84, v85
	v_cvt_pk_bf16_f32 v76, v76, v77
	v_cvt_pk_bf16_f32 v77, v90, v91
	global_store_dwordx4 v[98:99], v[74:77], off offset:256
	v_mov_b32_e32 v84, v177
	v_pk_mul_f32 v[80:81], v[84:85], v[80:81] op_sel_hi:[0,1]
	v_or_b32_e32 v74, 48, v138
	v_mad_i64_i32 v[74:75], s[10:11], v74, s42, v[130:131]
	v_lshl_add_u64 v[82:83], v[74:75], 0, v[132:133]
	v_pk_mul_f32 v[76:77], v[84:85], v[88:89] op_sel_hi:[0,1]
	v_pk_mul_f32 v[74:75], v[84:85], v[86:87] op_sel_hi:[0,1]
	v_pk_mul_f32 v[78:79], v[84:85], v[78:79] op_sel_hi:[0,1]
	v_cvt_pk_bf16_f32 v74, v74, v75
	v_cvt_pk_bf16_f32 v75, v76, v77
	v_cvt_pk_bf16_f32 v76, v78, v79
	v_cvt_pk_bf16_f32 v77, v80, v81
	global_store_dwordx4 v[82:83], v[74:77], off
	v_pk_mul_f32 v[72:73], v[84:85], v[72:73] op_sel_hi:[0,1]
	v_pk_mul_f32 v[70:71], v[84:85], v[70:71] op_sel_hi:[0,1]
	v_pk_mul_f32 v[74:75], v[84:85], v[68:69] op_sel_hi:[0,1]
	v_pk_mul_f32 v[68:69], v[84:85], v[66:67] op_sel_hi:[0,1]
	v_cvt_pk_bf16_f32 v66, v70, v71
	v_cvt_pk_bf16_f32 v67, v72, v73
	v_cvt_pk_bf16_f32 v68, v68, v69
	v_cvt_pk_bf16_f32 v69, v74, v75
	global_store_dwordx4 v[82:83], v[66:69], off offset:256
	v_pk_mul_f32 v[62:63], v[170:171], v[62:63] op_sel_hi:[0,1]
	v_pk_mul_f32 v[52:53], v[170:171], v[52:53] op_sel_hi:[0,1]
	v_add_u32_e32 v66, 0x80, v138
	v_mad_i64_i32 v[66:67], s[10:11], v66, s42, v[130:131]
	v_pk_mul_f32 v[68:69], v[170:171], v[60:61] op_sel_hi:[0,1]
	v_pk_mul_f32 v[60:61], v[170:171], v[58:59] op_sel_hi:[0,1]
	v_lshl_add_u64 v[66:67], v[66:67], 0, v[132:133]
	v_cvt_pk_bf16_f32 v58, v62, v63
	v_cvt_pk_bf16_f32 v59, v64, v65
	v_cvt_pk_bf16_f32 v60, v60, v61
	v_cvt_pk_bf16_f32 v61, v68, v69
	global_store_dwordx4 v[66:67], v[58:61], off
	v_pk_mul_f32 v[50:51], v[170:171], v[50:51] op_sel_hi:[0,1]
	v_pk_mul_f32 v[48:49], v[170:171], v[48:49] op_sel:[1,0]
	v_pk_mul_f32 v[58:59], v[170:171], v[44:45] op_sel_hi:[0,1]
	v_pk_mul_f32 v[44:45], v[170:171], v[42:43] op_sel_hi:[0,1]
	v_cvt_pk_bf16_f32 v42, v50, v51
	v_cvt_pk_bf16_f32 v43, v52, v53
	v_cvt_pk_bf16_f32 v44, v44, v45
	v_cvt_pk_bf16_f32 v45, v58, v59
	global_store_dwordx4 v[66:67], v[42:45], off offset:256
	v_pk_mul_f32 v[46:47], v[170:171], v[46:47] op_sel:[1,0]
	v_pk_mul_f32 v[36:37], v[170:171], v[36:37] op_sel:[1,0]
	v_add_u32_e32 v42, 0x90, v138
	v_mad_i64_i32 v[42:43], s[10:11], v42, s42, v[130:131]
	v_lshl_add_u64 v[50:51], v[42:43], 0, v[132:133]
	v_pk_mul_f32 v[44:45], v[170:171], v[56:57] op_sel:[1,0]
	v_pk_mul_f32 v[42:43], v[170:171], v[54:55] op_sel:[1,0]
	v_pk_mul_f32 v[34:35], v[170:171], v[34:35] op_sel:[1,0]
	v_cvt_pk_bf16_f32 v42, v42, v43
	v_cvt_pk_bf16_f32 v43, v44, v45
	v_cvt_pk_bf16_f32 v44, v46, v47
	v_cvt_pk_bf16_f32 v45, v48, v49
	global_store_dwordx4 v[50:51], v[42:45], off
	v_pk_mul_f32 v[32:33], v[174:175], v[32:33] op_sel_hi:[0,1]
	v_pk_mul_f32 v[30:31], v[174:175], v[30:31] op_sel_hi:[0,1]
	v_pk_mul_f32 v[42:43], v[170:171], v[28:29] op_sel:[1,0]
	v_pk_mul_f32 v[28:29], v[170:171], v[26:27] op_sel:[1,0]
	v_cvt_pk_bf16_f32 v26, v34, v35
	v_cvt_pk_bf16_f32 v27, v36, v37
	v_cvt_pk_bf16_f32 v28, v28, v29
	v_cvt_pk_bf16_f32 v29, v42, v43
	global_store_dwordx4 v[50:51], v[26:29], off offset:256
	v_pk_mul_f32 v[20:21], v[174:175], v[20:21] op_sel_hi:[0,1]
	v_pk_mul_f32 v[18:19], v[174:175], v[18:19] op_sel_hi:[0,1]
	v_add_u32_e32 v26, 0xa0, v138
	v_mad_i64_i32 v[26:27], s[10:11], v26, s42, v[130:131]
	v_lshl_add_u64 v[34:35], v[26:27], 0, v[132:133]
	v_pk_mul_f32 v[28:29], v[174:175], v[40:41] op_sel_hi:[0,1]
	v_pk_mul_f32 v[26:27], v[174:175], v[38:39] op_sel_hi:[0,1]
	v_cvt_pk_bf16_f32 v26, v26, v27
	v_cvt_pk_bf16_f32 v27, v28, v29
	v_cvt_pk_bf16_f32 v28, v30, v31
	v_cvt_pk_bf16_f32 v29, v32, v33
	global_store_dwordx4 v[34:35], v[26:29], off
	s_and_b64 vcc, exec, s[2:3]
	s_mov_b32 s47, s44
	v_pk_mul_f32 v[26:27], v[174:175], v[12:13] op_sel_hi:[0,1]
	v_pk_mul_f32 v[12:13], v[174:175], v[10:11] op_sel_hi:[0,1]
	v_cvt_pk_bf16_f32 v10, v18, v19
	v_cvt_pk_bf16_f32 v11, v20, v21
	v_cvt_pk_bf16_f32 v12, v12, v13
	v_cvt_pk_bf16_f32 v13, v26, v27
	global_store_dwordx4 v[34:35], v[10:13], off offset:256
	v_mov_b32_e32 v20, v175
	v_pk_mul_f32 v[16:17], v[20:21], v[16:17] op_sel_hi:[0,1]
	v_add_u32_e32 v10, 0xb0, v138
	v_mad_i64_i32 v[10:11], s[10:11], v10, s42, v[130:131]
	v_lshl_add_u64 v[18:19], v[10:11], 0, v[132:133]
	v_pk_mul_f32 v[12:13], v[20:21], v[24:25] op_sel_hi:[0,1]
	v_pk_mul_f32 v[10:11], v[20:21], v[22:23] op_sel_hi:[0,1]
	v_pk_mul_f32 v[14:15], v[20:21], v[14:15] op_sel_hi:[0,1]
	v_cvt_pk_bf16_f32 v10, v10, v11
	v_cvt_pk_bf16_f32 v11, v12, v13
	v_cvt_pk_bf16_f32 v12, v14, v15
	v_cvt_pk_bf16_f32 v13, v16, v17
	global_store_dwordx4 v[18:19], v[10:13], off
	v_pk_mul_f32 v[8:9], v[20:21], v[8:9] op_sel_hi:[0,1]
	v_pk_mul_f32 v[6:7], v[20:21], v[6:7] op_sel_hi:[0,1]
	v_pk_mul_f32 v[10:11], v[20:21], v[4:5] op_sel_hi:[0,1]
	v_pk_mul_f32 v[4:5], v[20:21], v[2:3] op_sel_hi:[0,1]
	v_cvt_pk_bf16_f32 v2, v6, v7
	v_cvt_pk_bf16_f32 v3, v8, v9
	v_cvt_pk_bf16_f32 v4, v4, v5
	v_cvt_pk_bf16_f32 v5, v10, v11
	s_mov_b32 s46, s43
	s_mov_b32 s51, s45
	s_mov_b32 s50, s33
	global_store_dwordx4 v[18:19], v[2:5], off offset:256
	s_cbranch_vccnz .LBB0_194

; #define PG8_STAGE_A(bufoff, soff, voff) do { _Pragma("unroll") for (int _i = 0; _i < 2; ++_i) \
;         __builtin_amdgcn_raw_ptr_buffer_load_lds(rsA, (LAS void*)(lds + (bufoff) + ldsw + _i * 8192), 16, (voff)[_i], (soff), 0, 0); } while (0)
; #define PG8_STAGE_B(bufoff, soff) do { _Pragma("unroll") for (int _i = 0; _i < 2; ++_i) \
;         __builtin_amdgcn_raw_ptr_buffer_load_lds(rsB, (LAS void*)(lds + (bufoff) + ldsw + _i * 8192), 16, voffB[_i], (soff), 0, 0); } while (0)
; #define PG8_LDA(dst, b, h) do { _Pragma("unroll") for (int m = 0; m < 4; ++m) dst[m] = PG8_LD8(lds + PG8_SA(b, h) + aoff + m * 2048); } while (0)
; #define PG8_LDB(dst, b, h) do { _Pragma("unroll") for (int n = 0; n < 2; ++n) dst[n] = PG8_LD8(lds + PG8_SB(b, h) + boff + n * 2048); } while (0)
; #define PG8_WAIT_V(n) asm volatile("s_waitcnt vmcnt(" #n ")" ::: "memory")
; #define PG8_WAIT_L(n) asm volatile("s_waitcnt lgkmcnt(" #n ")" ::: "memory")
; #define PG8_BAR __builtin_amdgcn_s_barrier()
; #define PG8_SCHED __builtin_amdgcn_sched_barrier(0)
; template <class Epi, class Sched, bool GATHER, bool ALIGN_EPI, bool SP2, bool FP8>
; __device__ __forceinline__ void gemm_phase(LAS unsigned char* lds, const Gemm g, const Sched& S, const Epi& E) {
;     ...
;         for (int t = 0; t < nt; t += 2) {
;             const bool last = (t == nt - 2);
;             if (last) pre = E.prefetch(cur, wr, wc, fr, fq);
;             const int a1 = cA + (t + 1) * kstep;
;             const int a2 = last ? nA : cA + (t + 2) * kstep, b2 = last ? nB : cB + (t + 2) * kstep;
;             const int a3 = a2 + kstep, b3 = b2 + kstep;
;             const u32x2 va20 = (GATHER && last) ? nvA0 : vA0, va21 = (GATHER && last) ? nvA1 : vA1;
;             if constexpr (SP2) {
;             PG8_LDB(B0, 0, 0); PG8_LDB(B1, 0, 1); PG8_SCHED; PG8_LDA(At, 0, 0); PG8_STAGE_A(PG8_SA(1, 1), a1, vA1);
;             PG8_WAIT_V(8); PG8_WAIT_L(0); PG8_BAR; PG8_MMA(0, 0, At, B0); PG8_MMA(0, 1, At, B1); PG8_BAR; PG8_SCHED;
;             PG8_LDA(At, 0, 1); PG8_STAGE_B(PG8_SB(0, 0), b2); PG8_STAGE_B(PG8_SB(0, 1), b2 + hstep); PG8_STAGE_A(PG8_SA(0, 0), a2, va20);
;             PG8_WAIT_V(8); PG8_WAIT_L(0); PG8_BAR; PG8_MMA(1, 0, At, B0); PG8_MMA(1, 1, At, B1); PG8_BAR; PG8_SCHED;
.LBB0_191:
	v_add_u32_e32 v130, 0x10000, v186
	v_add_u32_e32 v131, 0x14000, v186
	ds_read_b128 v[158:161], v130
	ds_read_b128 v[154:157], v130 offset:1024
	ds_read_b128 v[150:153], v130 offset:2048
	ds_read_b128 v[146:149], v130 offset:3072
	ds_read_b128 v[142:145], v131
	ds_read_b128 v[138:141], v131 offset:1024
	ds_read_b128 v[134:137], v131 offset:2048
	ds_read_b128 v[130:133], v131 offset:3072
	s_add_i32 s53, s50, 0x80
	s_and_b64 s[56:57], s[10:11], exec
	s_cselect_b32 s57, s48, s53
	s_or_b32 s53, s57, 0x80
	s_and_b64 s[10:11], s[10:11], exec
	s_cselect_b32 s56, s49, s51
	s_mov_b32 m0, s39
	ds_read_b128 v[188:191], v187
	ds_read_b128 v[192:195], v187 offset:1024
	ds_read_b128 v[196:199], v187 offset:2048
	ds_read_b128 v[200:203], v187 offset:3072
	ds_read_b128 v[204:207], v187 offset:4096
	ds_read_b128 v[208:211], v187 offset:5120
	ds_read_b128 v[212:215], v187 offset:6144
	ds_read_b128 v[216:219], v187 offset:7168
	buffer_load_dwordx4 v183, s[4:7], s50 offen lds
	s_mov_b32 m0, s40
	s_nop 0
	buffer_load_dwordx4 v184, s[4:7], s50 offen lds
	s_cmp_eq_u32 s52, 28
	s_cbranch_scc1 .Lp1w0_last
	s_cmp_lg_u32 s52, -2
	s_cbranch_scc1 .Lp1w0_norm
	s_cmp_eq_u32 s99, 0
	s_cbranch_scc1 .Lp1w0_norm
	s_waitcnt vmcnt(24)
	s_branch .Lp1w0_join
.Lp1w0_last:
	s_waitcnt vmcnt(16)
	s_branch .Lp1w0_join
.Lp1w0_norm:
	s_waitcnt vmcnt(8)
.Lp1w0_join:
	s_waitcnt lgkmcnt(0)
	s_barrier
	s_setprio 1
	s_waitcnt lgkmcnt(7)
	v_mfma_f32_16x16x32_bf16 v[126:129], v[158:161], v[188:191], v[126:129]
	s_waitcnt lgkmcnt(6)
	v_mfma_f32_16x16x32_bf16 v[126:129], v[154:157], v[192:195], v[126:129]
	v_mfma_f32_16x16x32_bf16 v[122:125], v[150:153], v[188:191], v[122:125]
	s_nop 0
	v_mfma_f32_16x16x32_bf16 v[122:125], v[146:149], v[192:195], v[122:125]
	s_waitcnt lgkmcnt(5)
	v_mfma_f32_16x16x32_bf16 v[118:121], v[158:161], v[196:199], v[118:121]
	s_waitcnt lgkmcnt(4)
	v_mfma_f32_16x16x32_bf16 v[118:121], v[154:157], v[200:203], v[118:121]
	v_mfma_f32_16x16x32_bf16 v[110:113], v[150:153], v[196:199], v[110:113]
	s_nop 0
	v_mfma_f32_16x16x32_bf16 v[110:113], v[146:149], v[200:203], v[110:113]
	s_waitcnt lgkmcnt(3)
	v_mfma_f32_16x16x32_bf16 v[102:105], v[158:161], v[204:207], v[102:105]
	s_waitcnt lgkmcnt(2)
	v_mfma_f32_16x16x32_bf16 v[102:105], v[154:157], v[208:211], v[102:105]
	v_mfma_f32_16x16x32_bf16 v[94:97], v[150:153], v[204:207], v[94:97]
	s_nop 0
	v_mfma_f32_16x16x32_bf16 v[94:97], v[146:149], v[208:211], v[94:97]
	s_waitcnt lgkmcnt(1)
	v_mfma_f32_16x16x32_bf16 v[86:89], v[158:161], v[212:215], v[86:89]
	s_waitcnt lgkmcnt(0)
	v_mfma_f32_16x16x32_bf16 v[86:89], v[154:157], v[216:219], v[86:89]
	v_mfma_f32_16x16x32_bf16 v[78:81], v[150:153], v[212:215], v[78:81]
	s_nop 0
	v_mfma_f32_16x16x32_bf16 v[78:81], v[146:149], v[216:219], v[78:81]
	s_setprio 0
	s_setprio 1
	v_mfma_f32_16x16x32_bf16 v[114:117], v[142:145], v[188:191], v[114:117]
	s_nop 0
	v_mfma_f32_16x16x32_bf16 v[114:117], v[138:141], v[192:195], v[114:117]
	v_mfma_f32_16x16x32_bf16 v[106:109], v[134:137], v[188:191], v[106:109]
	s_nop 0
	v_mfma_f32_16x16x32_bf16 v[106:109], v[130:133], v[192:195], v[106:109]
	v_mfma_f32_16x16x32_bf16 v[98:101], v[142:145], v[196:199], v[98:101]
	s_nop 0
	v_mfma_f32_16x16x32_bf16 v[98:101], v[138:141], v[200:203], v[98:101]
	v_mfma_f32_16x16x32_bf16 v[90:93], v[134:137], v[196:199], v[90:93]
	s_nop 0
	v_mfma_f32_16x16x32_bf16 v[90:93], v[130:133], v[200:203], v[90:93]
	v_mfma_f32_16x16x32_bf16 v[82:85], v[142:145], v[204:207], v[82:85]
	s_nop 0
	v_mfma_f32_16x16x32_bf16 v[82:85], v[138:141], v[208:211], v[82:85]
	v_mfma_f32_16x16x32_bf16 v[74:77], v[134:137], v[204:207], v[74:77]
	s_nop 0
	v_mfma_f32_16x16x32_bf16 v[74:77], v[130:133], v[208:211], v[74:77]
	v_mfma_f32_16x16x32_bf16 v[70:73], v[142:145], v[212:215], v[70:73]
	s_nop 0
	v_mfma_f32_16x16x32_bf16 v[70:73], v[138:141], v[216:219], v[70:73]
	v_mfma_f32_16x16x32_bf16 v[66:69], v[134:137], v[212:215], v[66:69]
	s_nop 0
	v_mfma_f32_16x16x32_bf16 v[66:69], v[130:133], v[216:219], v[66:69]
	s_setprio 0
	s_barrier
	s_mov_b32 m0, s23
	s_mov_b32 s10, s6
	s_mov_b32 s11, s7
	ds_read_b128 v[188:191], v187 offset:16384
	ds_read_b128 v[192:195], v187 offset:17408
	ds_read_b128 v[196:199], v187 offset:18432
	ds_read_b128 v[200:203], v187 offset:19456
	ds_read_b128 v[204:207], v187 offset:20480
	ds_read_b128 v[208:211], v187 offset:21504
	ds_read_b128 v[212:215], v187 offset:22528
	ds_read_b128 v[216:219], v187 offset:23552
	buffer_load_dwordx4 v165, s[8:11], s56 offen lds
	s_mov_b32 m0, s24
	s_add_i32 s58, s56, 0x80000
	buffer_load_dwordx4 v180, s[8:11], s56 offen lds
	s_mov_b32 m0, s25
	s_nop 0
	buffer_load_dwordx4 v165, s[8:11], s58 offen lds
	s_mov_b32 m0, s26
	s_nop 0
	buffer_load_dwordx4 v180, s[8:11], s58 offen lds
	s_mov_b32 m0, s22
	s_nop 0
	buffer_load_dwordx4 v181, s[4:7], s57 offen lds
	s_mov_b32 m0, s27
	s_nop 0
	buffer_load_dwordx4 v182, s[4:7], s57 offen lds
	s_cmp_eq_u32 s52, 28
	s_cbranch_scc1 .Lp1w1_last
	s_cmp_lg_u32 s52, -2
	s_cbranch_scc1 .Lp1w1_norm
	s_cmp_eq_u32 s99, 0
	s_cbranch_scc1 .Lp1w1_norm
	s_waitcnt vmcnt(24)
	s_branch .Lp1w1_join

; #define PG8_STAGE_A(bufoff, soff, voff) do { _Pragma("unroll") for (int _i = 0; _i < 2; ++_i) \
;         __builtin_amdgcn_raw_ptr_buffer_load_lds(rsA, (LAS void*)(lds + (bufoff) + ldsw + _i * 8192), 16, (voff)[_i], (soff), 0, 0); } while (0)
; #define PG8_LDA(dst, b, h) do { _Pragma("unroll") for (int m = 0; m < 4; ++m) dst[m] = PG8_LD8(lds + PG8_SA(b, h) + aoff + m * 2048); } while (0)
; #define PG8_LDB(dst, b, h) do { _Pragma("unroll") for (int n = 0; n < 2; ++n) dst[n] = PG8_LD8(lds + PG8_SB(b, h) + boff + n * 2048); } while (0)
; #define PG8_WAIT_V(n) asm volatile("s_waitcnt vmcnt(" #n ")" ::: "memory")
; #define PG8_WAIT_L(n) asm volatile("s_waitcnt lgkmcnt(" #n ")" ::: "memory")
; #define PG8_BAR __builtin_amdgcn_s_barrier()
; #define PG8_SCHED __builtin_amdgcn_sched_barrier(0)
; template <class Epi, class Sched, bool GATHER, bool ALIGN_EPI, bool SP2, bool FP8>
; __device__ __forceinline__ void gemm_phase(LAS unsigned char* lds, const Gemm g, const Sched& S, const Epi& E) {
;     ...
;             PG8_WAIT_V(8); PG8_WAIT_L(0); PG8_BAR; PG8_MMA(1, 0, At, B0); PG8_MMA(1, 1, At, B1); PG8_BAR; PG8_SCHED;
;             PG8_LDB(B0, 1, 0); PG8_LDB(B1, 1, 1); PG8_SCHED; PG8_LDA(At, 1, 0); PG8_STAGE_A(PG8_SA(0, 1), a2, va21);
;             PG8_WAIT_V(8); PG8_WAIT_L(0); PG8_BAR; PG8_MMA(0, 0, At, B0); PG8_MMA(0, 1, At, B1); PG8_BAR; PG8_SCHED;
.Lp1w1_join:
	s_waitcnt lgkmcnt(0)
	s_barrier
	s_setprio 1
	s_waitcnt lgkmcnt(7)
	v_mfma_f32_16x16x32_bf16 v[62:65], v[158:161], v[188:191], v[62:65]
	s_waitcnt lgkmcnt(6)
	v_mfma_f32_16x16x32_bf16 v[62:65], v[154:157], v[192:195], v[62:65]
	v_mfma_f32_16x16x32_bf16 v[58:61], v[150:153], v[188:191], v[58:61]
	s_nop 0
	v_mfma_f32_16x16x32_bf16 v[58:61], v[146:149], v[192:195], v[58:61]
	s_waitcnt lgkmcnt(5)
	v_mfma_f32_16x16x32_bf16 v[54:57], v[158:161], v[196:199], v[54:57]
	s_waitcnt lgkmcnt(4)
	v_mfma_f32_16x16x32_bf16 v[54:57], v[154:157], v[200:203], v[54:57]
	v_mfma_f32_16x16x32_bf16 v[46:49], v[150:153], v[196:199], v[46:49]
	s_nop 0
	v_mfma_f32_16x16x32_bf16 v[46:49], v[146:149], v[200:203], v[46:49]
	s_waitcnt lgkmcnt(3)
	v_mfma_f32_16x16x32_bf16 v[38:41], v[158:161], v[204:207], v[38:41]
	s_waitcnt lgkmcnt(2)
	v_mfma_f32_16x16x32_bf16 v[38:41], v[154:157], v[208:211], v[38:41]
	v_mfma_f32_16x16x32_bf16 v[30:33], v[150:153], v[204:207], v[30:33]
	s_nop 0
	v_mfma_f32_16x16x32_bf16 v[30:33], v[146:149], v[208:211], v[30:33]
	s_waitcnt lgkmcnt(1)
	v_mfma_f32_16x16x32_bf16 v[22:25], v[158:161], v[212:215], v[22:25]
	s_waitcnt lgkmcnt(0)
	v_mfma_f32_16x16x32_bf16 v[22:25], v[154:157], v[216:219], v[22:25]
	v_mfma_f32_16x16x32_bf16 v[14:17], v[150:153], v[212:215], v[14:17]
	s_nop 0
	v_mfma_f32_16x16x32_bf16 v[14:17], v[146:149], v[216:219], v[14:17]
	s_setprio 0
	s_setprio 1
	v_mfma_f32_16x16x32_bf16 v[50:53], v[142:145], v[188:191], v[50:53]
	s_nop 0
	v_mfma_f32_16x16x32_bf16 v[50:53], v[138:141], v[192:195], v[50:53]
	v_mfma_f32_16x16x32_bf16 v[42:45], v[134:137], v[188:191], v[42:45]
	s_nop 0
	v_mfma_f32_16x16x32_bf16 v[42:45], v[130:133], v[192:195], v[42:45]
	v_mfma_f32_16x16x32_bf16 v[34:37], v[142:145], v[196:199], v[34:37]
	s_nop 0
	v_mfma_f32_16x16x32_bf16 v[34:37], v[138:141], v[200:203], v[34:37]
	v_mfma_f32_16x16x32_bf16 v[26:29], v[134:137], v[196:199], v[26:29]
	s_nop 0
	v_mfma_f32_16x16x32_bf16 v[26:29], v[130:133], v[200:203], v[26:29]
	v_mfma_f32_16x16x32_bf16 v[18:21], v[142:145], v[204:207], v[18:21]
	s_nop 0
	v_mfma_f32_16x16x32_bf16 v[18:21], v[138:141], v[208:211], v[18:21]
	v_mfma_f32_16x16x32_bf16 v[10:13], v[134:137], v[204:207], v[10:13]
	s_nop 0
	v_mfma_f32_16x16x32_bf16 v[10:13], v[130:133], v[208:211], v[10:13]
	v_mfma_f32_16x16x32_bf16 v[6:9], v[142:145], v[212:215], v[6:9]
	s_nop 0
	v_mfma_f32_16x16x32_bf16 v[6:9], v[138:141], v[216:219], v[6:9]
	v_mfma_f32_16x16x32_bf16 v[2:5], v[134:137], v[212:215], v[2:5]
	s_nop 0
	v_mfma_f32_16x16x32_bf16 v[2:5], v[130:133], v[216:219], v[2:5]
	s_setprio 0
	s_barrier
	v_add_u32_e32 v142, 0x18000, v186
	v_add_u32_e32 v158, 0x1c000, v186
	ds_read_b128 v[130:133], v142
	ds_read_b128 v[134:137], v142 offset:1024
	ds_read_b128 v[138:141], v142 offset:2048
	ds_read_b128 v[142:145], v142 offset:3072
	ds_read_b128 v[146:149], v158
	ds_read_b128 v[150:153], v158 offset:1024
	ds_read_b128 v[154:157], v158 offset:2048
	ds_read_b128 v[158:161], v158 offset:3072
	s_mov_b32 m0, s28
	ds_read_b128 v[188:191], v187 offset:32768
	ds_read_b128 v[192:195], v187 offset:33792
	ds_read_b128 v[196:199], v187 offset:34816
	ds_read_b128 v[200:203], v187 offset:35840
	ds_read_b128 v[204:207], v187 offset:36864
	ds_read_b128 v[208:211], v187 offset:37888
	ds_read_b128 v[212:215], v187 offset:38912
	ds_read_b128 v[216:219], v187 offset:39936
	buffer_load_dwordx4 v183, s[4:7], s57 offen lds
	s_mov_b32 m0, s29
	s_nop 0
	buffer_load_dwordx4 v184, s[4:7], s57 offen lds
	s_waitcnt vmcnt(8)
	s_waitcnt lgkmcnt(0)
	s_barrier
	s_setprio 1
	s_waitcnt lgkmcnt(7)
	v_mfma_f32_16x16x32_bf16 v[126:129], v[130:133], v[188:191], v[126:129]
	s_waitcnt lgkmcnt(6)
	v_mfma_f32_16x16x32_bf16 v[126:129], v[134:137], v[192:195], v[126:129]
	v_mfma_f32_16x16x32_bf16 v[122:125], v[138:141], v[188:191], v[122:125]
	s_nop 0
	v_mfma_f32_16x16x32_bf16 v[122:125], v[142:145], v[192:195], v[122:125]
	s_waitcnt lgkmcnt(5)
	v_mfma_f32_16x16x32_bf16 v[118:121], v[130:133], v[196:199], v[118:121]
	s_waitcnt lgkmcnt(4)
	v_mfma_f32_16x16x32_bf16 v[118:121], v[134:137], v[200:203], v[118:121]
	v_mfma_f32_16x16x32_bf16 v[110:113], v[138:141], v[196:199], v[110:113]
	s_nop 0
	v_mfma_f32_16x16x32_bf16 v[110:113], v[142:145], v[200:203], v[110:113]
	s_waitcnt lgkmcnt(3)
	v_mfma_f32_16x16x32_bf16 v[102:105], v[130:133], v[204:207], v[102:105]
	s_waitcnt lgkmcnt(2)
	v_mfma_f32_16x16x32_bf16 v[102:105], v[134:137], v[208:211], v[102:105]
	v_mfma_f32_16x16x32_bf16 v[94:97], v[138:141], v[204:207], v[94:97]
	s_nop 0
	v_mfma_f32_16x16x32_bf16 v[94:97], v[142:145], v[208:211], v[94:97]
	s_waitcnt lgkmcnt(1)
	v_mfma_f32_16x16x32_bf16 v[86:89], v[130:133], v[212:215], v[86:89]
	s_waitcnt lgkmcnt(0)
	v_mfma_f32_16x16x32_bf16 v[86:89], v[134:137], v[216:219], v[86:89]
	v_mfma_f32_16x16x32_bf16 v[78:81], v[138:141], v[212:215], v[78:81]
	s_nop 0
	v_mfma_f32_16x16x32_bf16 v[78:81], v[142:145], v[216:219], v[78:81]
	s_setprio 0
	s_setprio 1
	v_mfma_f32_16x16x32_bf16 v[114:117], v[146:149], v[188:191], v[114:117]
	s_nop 0
	v_mfma_f32_16x16x32_bf16 v[114:117], v[150:153], v[192:195], v[114:117]
	v_mfma_f32_16x16x32_bf16 v[106:109], v[154:157], v[188:191], v[106:109]
	s_nop 0
	v_mfma_f32_16x16x32_bf16 v[106:109], v[158:161], v[192:195], v[106:109]
	v_mfma_f32_16x16x32_bf16 v[98:101], v[146:149], v[196:199], v[98:101]
	s_nop 0
	v_mfma_f32_16x16x32_bf16 v[98:101], v[150:153], v[200:203], v[98:101]
	v_mfma_f32_16x16x32_bf16 v[90:93], v[154:157], v[196:199], v[90:93]
	s_nop 0
	v_mfma_f32_16x16x32_bf16 v[90:93], v[158:161], v[200:203], v[90:93]
	v_mfma_f32_16x16x32_bf16 v[82:85], v[146:149], v[204:207], v[82:85]
	s_nop 0
	v_mfma_f32_16x16x32_bf16 v[82:85], v[150:153], v[208:211], v[82:85]
	v_mfma_f32_16x16x32_bf16 v[74:77], v[154:157], v[204:207], v[74:77]
	s_nop 0
	v_mfma_f32_16x16x32_bf16 v[74:77], v[158:161], v[208:211], v[74:77]
	v_mfma_f32_16x16x32_bf16 v[70:73], v[146:149], v[212:215], v[70:73]
	s_nop 0
	v_mfma_f32_16x16x32_bf16 v[70:73], v[150:153], v[216:219], v[70:73]
	v_mfma_f32_16x16x32_bf16 v[66:69], v[154:157], v[212:215], v[66:69]
	s_nop 0
	v_mfma_f32_16x16x32_bf16 v[66:69], v[158:161], v[216:219], v[66:69]
	s_setprio 0
	s_barrier
; #define PG8_STAGE_A(bufoff, soff, voff) do { _Pragma("unroll") for (int _i = 0; _i < 2; ++_i) \
;         __builtin_amdgcn_raw_ptr_buffer_load_lds(rsA, (LAS void*)(lds + (bufoff) + ldsw + _i * 8192), 16, (voff)[_i], (soff), 0, 0); } while (0)
; #define PG8_STAGE_B(bufoff, soff) do { _Pragma("unroll") for (int _i = 0; _i < 2; ++_i) \
;         __builtin_amdgcn_raw_ptr_buffer_load_lds(rsB, (LAS void*)(lds + (bufoff) + ldsw + _i * 8192), 16, voffB[_i], (soff), 0, 0); } while (0)
; #define PG8_LDA(dst, b, h) do { _Pragma("unroll") for (int m = 0; m < 4; ++m) dst[m] = PG8_LD8(lds + PG8_SA(b, h) + aoff + m * 2048); } while (0)
; #define PG8_WAIT_V(n) asm volatile("s_waitcnt vmcnt(" #n ")" ::: "memory")
; #define PG8_WAIT_L(n) asm volatile("s_waitcnt lgkmcnt(" #n ")" ::: "memory")
; #define PG8_BAR __builtin_amdgcn_s_barrier()
; #define PG8_SCHED __builtin_amdgcn_sched_barrier(0)
; template <class Epi, class Sched, bool GATHER, bool ALIGN_EPI, bool SP2, bool FP8>
; __device__ __forceinline__ void gemm_phase(LAS unsigned char* lds, const Gemm g, const Sched& S, const Epi& E) {
;     ...
;             PG8_LDA(At, 1, 1); PG8_STAGE_B(PG8_SB(1, 0), b3); PG8_STAGE_B(PG8_SB(1, 1), b3 + hstep); PG8_STAGE_A(PG8_SA(1, 0), a3, va20);
;             PG8_WAIT_V(8); PG8_WAIT_L(0); PG8_BAR; PG8_MMA(1, 0, At, B0); PG8_MMA(1, 1, At, B1); PG8_BAR; PG8_SCHED;
	s_mov_b32 m0, s31
	s_or_b32 s57, s56, 0x80
	ds_read_b128 v[188:191], v187 offset:49152
	ds_read_b128 v[192:195], v187 offset:50176
	ds_read_b128 v[196:199], v187 offset:51200
	ds_read_b128 v[200:203], v187 offset:52224
	ds_read_b128 v[204:207], v187 offset:53248
	ds_read_b128 v[208:211], v187 offset:54272
	ds_read_b128 v[212:215], v187 offset:55296
	ds_read_b128 v[216:219], v187 offset:56320
	buffer_load_dwordx4 v165, s[8:11], s57 offen lds
	s_mov_b32 m0, s34
	s_add_i32 s56, s56, 0x80080
	buffer_load_dwordx4 v180, s[8:11], s57 offen lds
	s_mov_b32 m0, s37
	s_nop 0
	buffer_load_dwordx4 v165, s[8:11], s56 offen lds
	s_mov_b32 m0, s38
	s_nop 0
	buffer_load_dwordx4 v180, s[8:11], s56 offen lds
	s_mov_b32 m0, s35
	s_nop 0
	buffer_load_dwordx4 v181, s[4:7], s53 offen lds
	s_mov_b32 m0, s36
	s_nop 0
	buffer_load_dwordx4 v182, s[4:7], s53 offen lds
	s_waitcnt vmcnt(8)
	s_waitcnt lgkmcnt(0)
	s_barrier
	s_setprio 1
	s_waitcnt lgkmcnt(7)
	v_mfma_f32_16x16x32_bf16 v[62:65], v[130:133], v[188:191], v[62:65]
	s_waitcnt lgkmcnt(6)
	v_mfma_f32_16x16x32_bf16 v[62:65], v[134:137], v[192:195], v[62:65]
	v_mfma_f32_16x16x32_bf16 v[58:61], v[138:141], v[188:191], v[58:61]
	s_nop 0
	v_mfma_f32_16x16x32_bf16 v[58:61], v[142:145], v[192:195], v[58:61]
	s_waitcnt lgkmcnt(5)
	v_mfma_f32_16x16x32_bf16 v[54:57], v[130:133], v[196:199], v[54:57]
	s_waitcnt lgkmcnt(4)
	v_mfma_f32_16x16x32_bf16 v[54:57], v[134:137], v[200:203], v[54:57]
	v_mfma_f32_16x16x32_bf16 v[46:49], v[138:141], v[196:199], v[46:49]
	s_nop 0
	v_mfma_f32_16x16x32_bf16 v[46:49], v[142:145], v[200:203], v[46:49]
	s_waitcnt lgkmcnt(3)
	v_mfma_f32_16x16x32_bf16 v[38:41], v[130:133], v[204:207], v[38:41]
	s_waitcnt lgkmcnt(2)
	v_mfma_f32_16x16x32_bf16 v[38:41], v[134:137], v[208:211], v[38:41]
	v_mfma_f32_16x16x32_bf16 v[30:33], v[138:141], v[204:207], v[30:33]
	s_nop 0
	v_mfma_f32_16x16x32_bf16 v[30:33], v[142:145], v[208:211], v[30:33]
	s_waitcnt lgkmcnt(1)
	v_mfma_f32_16x16x32_bf16 v[22:25], v[130:133], v[212:215], v[22:25]
	s_waitcnt lgkmcnt(0)
	v_mfma_f32_16x16x32_bf16 v[22:25], v[134:137], v[216:219], v[22:25]
	v_mfma_f32_16x16x32_bf16 v[14:17], v[138:141], v[212:215], v[14:17]
	s_nop 0
	v_mfma_f32_16x16x32_bf16 v[14:17], v[142:145], v[216:219], v[14:17]
	s_setprio 0
	s_setprio 1
	v_mfma_f32_16x16x32_bf16 v[50:53], v[146:149], v[188:191], v[50:53]
	s_nop 0
	v_mfma_f32_16x16x32_bf16 v[50:53], v[150:153], v[192:195], v[50:53]
	v_mfma_f32_16x16x32_bf16 v[42:45], v[154:157], v[188:191], v[42:45]
	s_nop 0
	v_mfma_f32_16x16x32_bf16 v[42:45], v[158:161], v[192:195], v[42:45]
	v_mfma_f32_16x16x32_bf16 v[34:37], v[146:149], v[196:199], v[34:37]
	s_nop 0
	v_mfma_f32_16x16x32_bf16 v[34:37], v[150:153], v[200:203], v[34:37]
	v_mfma_f32_16x16x32_bf16 v[26:29], v[154:157], v[196:199], v[26:29]
	s_nop 0
	v_mfma_f32_16x16x32_bf16 v[26:29], v[158:161], v[200:203], v[26:29]
	v_mfma_f32_16x16x32_bf16 v[18:21], v[146:149], v[204:207], v[18:21]
	s_nop 0
	v_mfma_f32_16x16x32_bf16 v[18:21], v[150:153], v[208:211], v[18:21]
	v_mfma_f32_16x16x32_bf16 v[10:13], v[154:157], v[204:207], v[10:13]
	s_nop 0
	v_mfma_f32_16x16x32_bf16 v[10:13], v[158:161], v[208:211], v[10:13]
	v_mfma_f32_16x16x32_bf16 v[6:9], v[146:149], v[212:215], v[6:9]
	s_nop 0
	v_mfma_f32_16x16x32_bf16 v[6:9], v[150:153], v[216:219], v[6:9]
	v_mfma_f32_16x16x32_bf16 v[2:5], v[154:157], v[212:215], v[2:5]
	s_nop 0
	v_mfma_f32_16x16x32_bf16 v[2:5], v[158:161], v[216:219], v[2:5]
	s_setprio 0
	s_barrier
	s_add_i32 s52, s52, 2
	s_addk_i32 s50, 0x100
	s_addk_i32 s51, 0x100
	s_cmp_gt_u32 s52, 29
	s_cbranch_scc1 .LBB0_187

; #define LAS __attribute__((address_space(3)))
; __device__ __forceinline__ void moe_tables(const Params& p, Frame& F) {
;     LAS int* tile0 = (LAS int*)(F.lds + L_TILE0); LAS int* cnt = (LAS int*)(F.lds + L_CNT);
;     if (F.tid < 64) {
;         const unsigned* gcnt = (const unsigned*)(p.ws + WS_CTL) + CW_CNT; const int e = F.tid & 31;
;         const int c = (int)__hip_atomic_load(gcnt + e, __ATOMIC_RELAXED, __HIP_MEMORY_SCOPE_AGENT); const int nt = (c + 255) >> 8;
;         int inc = nt;
; #pragma unroll
;         for (int o = 1; o < 32; o <<= 1) { const int v = __shfl_up(inc, o, 32); if (e >= o) inc += v; }
;         if (F.tid < 32) { cnt[e] = c; tile0[e] = inc - nt; if (e == NEXP - 1) tile0[NEXP] = inc; }
;     }
;     __syncthreads();
; }
; __global__ void __launch_bounds__(512, 2) hymba_fwd(Params p) {
;     ...
;     if (IN(8)) {
;         moe_tables(p, F);
;         pg8::Gemm g{(const bf16_t*)(ws + WS_ACT), (const bf16_t*)(ws + WS_WDN), DFF / 2};
;         pg8::MoeOrder S; S.init((const LAS int*)(F.lds + L_TILE0), (const LAS int*)(F.lds + L_CNT), (const int*)(ws + WS_LTOK), 8, F.G, (int)blockIdx.x);
.LBB0_991:
	s_mov_b32 s99, 0
	v_readlane_b32 s4, v245, 4
	s_cmp_lt_i32 s4, 9
	s_cselect_b64 s[2:3], -1, 0
	s_and_b64 s[0:1], s[2:3], s[0:1]
	s_andn2_b64 vcc, exec, s[0:1]
	v_cmp_gt_u32_e64 s[0:1], 64, v0
	v_readlane_b32 s5, v245, 5
	v_readlane_b32 s6, v245, 6
	v_readlane_b32 s7, v245, 7
	s_cbranch_vccnz .LBB0_1014
	s_and_saveexec_b64 s[4:5], s[0:1]
	s_cbranch_execz .LBB0_996
	v_and_b32_e32 v1, 31, v0
	s_waitcnt vmcnt(0)
	v_lshlrev_b32_e32 v2, 2, v1
	global_load_dword v2, v2, s[96:97] offset:256 sc1
	v_mbcnt_lo_u32_b32 v3, -1, 0
	v_mbcnt_hi_u32_b32 v4, -1, v3
	v_and_b32_e32 v5, 0x60, v4
	v_add_u32_e32 v3, -1, v4
	v_cmp_lt_i32_e32 vcc, v3, v5
	v_add_u32_e32 v6, -2, v4
	v_add_u32_e32 v7, -4, v4
	v_cndmask_b32_e32 v3, v3, v4, vcc
	v_lshlrev_b32_e32 v9, 2, v3
	v_cmp_lt_i32_e32 vcc, v6, v5
	v_add_u32_e32 v8, -8, v4
	s_waitcnt vmcnt(0)
	v_add_u32_e32 v3, 0xff, v2
	v_ashrrev_i32_e32 v3, 8, v3
	ds_bpermute_b32 v9, v9, v3
	v_cndmask_b32_e32 v6, v6, v4, vcc
	v_cmp_ne_u32_e32 vcc, 0, v1
	v_lshlrev_b32_e32 v6, 2, v6
	s_waitcnt lgkmcnt(0)
	v_cndmask_b32_e32 v9, 0, v9, vcc
	v_add_u32_e32 v9, v9, v3
	ds_bpermute_b32 v6, v6, v9
	v_cmp_lt_i32_e32 vcc, v7, v5
	s_nop 1
	v_cndmask_b32_e32 v7, v7, v4, vcc
	v_cmp_lt_u32_e32 vcc, 1, v1
	v_lshlrev_b32_e32 v7, 2, v7
	s_waitcnt lgkmcnt(0)
	v_cndmask_b32_e32 v6, 0, v6, vcc
	v_add_u32_e32 v6, v6, v9
	ds_bpermute_b32 v7, v7, v6
	v_cmp_lt_i32_e32 vcc, v8, v5
	s_nop 1
	v_cndmask_b32_e32 v8, v8, v4, vcc
	v_cmp_lt_u32_e32 vcc, 3, v1
	v_lshlrev_b32_e32 v8, 2, v8
	s_waitcnt lgkmcnt(0)
	v_cndmask_b32_e32 v7, 0, v7, vcc
	v_add_u32_e32 v6, v7, v6
	ds_bpermute_b32 v7, v8, v6
	v_add_u32_e32 v8, -16, v4
	v_cmp_lt_i32_e32 vcc, v8, v5
	s_nop 1
	v_cndmask_b32_e32 v5, v8, v4, vcc
	v_cmp_lt_u32_e32 vcc, 7, v1
	v_lshlrev_b32_e32 v5, 2, v5
	s_waitcnt lgkmcnt(0)
	v_cndmask_b32_e32 v4, 0, v7, vcc
	v_add_u32_e32 v4, v4, v6
	ds_bpermute_b32 v5, v5, v4
	v_cmp_gt_u32_e32 vcc, 32, v0
	s_and_b64 exec, exec, vcc
	s_cbranch_execz .LBB0_996
	v_cmp_lt_u32_e32 vcc, 15, v1
	s_waitcnt lgkmcnt(0)
	s_nop 0
	v_cndmask_b32_e32 v5, 0, v5, vcc
	v_add_u32_e32 v4, v5, v4
	v_lshl_add_u32 v5, v1, 2, 0
	v_add_u32_e32 v6, 0x27e00, v5
	ds_write_b32 v6, v2
	v_sub_u32_e32 v2, v4, v3
	v_add_u32_e32 v3, 0x27d00, v5
	v_cmp_eq_u32_e32 vcc, 31, v1
	ds_write_b32 v3, v2
	s_and_b64 exec, exec, vcc
	s_add_i32 s0, 0, 0x27d80
	v_mov_b32_e32 v1, s0
	ds_write_b32 v1, v4

; #define PG8_STAGE_A(bufoff, soff, voff) do { _Pragma("unroll") for (int _i = 0; _i < 2; ++_i) \
;         __builtin_amdgcn_raw_ptr_buffer_load_lds(rsA, (LAS void*)(lds + (bufoff) + ldsw + _i * 8192), 16, (voff)[_i], (soff), 0, 0); } while (0)
; #define PG8_LDA(dst, b, h) do { _Pragma("unroll") for (int m = 0; m < 4; ++m) dst[m] = PG8_LD8(lds + PG8_SA(b, h) + aoff + m * 2048); } while (0)
; #define PG8_LDB(dst, b, h) do { _Pragma("unroll") for (int n = 0; n < 2; ++n) dst[n] = PG8_LD8(lds + PG8_SB(b, h) + boff + n * 2048); } while (0)
; #define PG8_WAIT_V(n) asm volatile("s_waitcnt vmcnt(" #n ")" ::: "memory")
; #define PG8_WAIT_L(n) asm volatile("s_waitcnt lgkmcnt(" #n ")" ::: "memory")
; #define PG8_BAR __builtin_amdgcn_s_barrier()
; #define PG8_SCHED __builtin_amdgcn_sched_barrier(0)
; template <class Epi, class Sched, bool GATHER, bool ALIGN_EPI, bool SP2, bool FP8>
; __device__ __forceinline__ void gemm_phase(LAS unsigned char* lds, const Gemm g, const Sched& S, const Epi& E) {
;     ...
;         for (int t = 0; t < nt; t += 2) {
;             const bool last = (t == nt - 2);
;             if (last) pre = E.prefetch(cur, wr, wc, fr, fq);
;             const int a1 = cA + (t + 1) * kstep;
;             const int a2 = last ? nA : cA + (t + 2) * kstep, b2 = last ? nB : cB + (t + 2) * kstep;
;             const int a3 = a2 + kstep, b3 = b2 + kstep;
;             const u32x2 va20 = (GATHER && last) ? nvA0 : vA0, va21 = (GATHER && last) ? nvA1 : vA1;
;             if constexpr (SP2) {
;             PG8_LDB(B0, 0, 0); PG8_LDB(B1, 0, 1); PG8_SCHED; PG8_LDA(At, 0, 0); PG8_STAGE_A(PG8_SA(1, 1), a1, vA1);
;             PG8_WAIT_V(8); PG8_WAIT_L(0); PG8_BAR; PG8_MMA(0, 0, At, B0); PG8_MMA(0, 1, At, B1); PG8_BAR; PG8_SCHED;
.LBB0_1005:
	s_add_i32 s74, s69, 0x80
	s_and_b64 s[72:73], s[10:11], exec
	s_cselect_b32 s74, s33, s74
	s_or_b32 s73, s74, 0x80
	s_and_b64 s[10:11], s[10:11], exec
	s_cselect_b32 s72, s68, s70
	s_mov_b32 s10, s6
	s_mov_b32 s11, s7
	v_add_u32_e32 v14, 0x10000, v175
	ds_read_b128 v[2:5], v14
	ds_read_b128 v[6:9], v14 offset:1024
	ds_read_b128 v[10:13], v14 offset:2048
	ds_read_b128 v[14:17], v14 offset:3072
	v_add_u32_e32 v177, 0x14000, v175
	ds_read_b128 v[210:213], v177
	ds_read_b128 v[214:217], v177 offset:1024
	ds_read_b128 v[218:221], v177 offset:2048
	ds_read_b128 v[222:225], v177 offset:3072
	ds_read_b128 v[178:181], v176
	ds_read_b128 v[182:185], v176 offset:1024
	ds_read_b128 v[186:189], v176 offset:2048
	ds_read_b128 v[190:193], v176 offset:3072
	ds_read_b128 v[194:197], v176 offset:4096
	ds_read_b128 v[198:201], v176 offset:5120
	ds_read_b128 v[202:205], v176 offset:6144
	ds_read_b128 v[206:209], v176 offset:7168
	s_mov_b32 m0, s36
	s_nop 0
	buffer_load_dwordx4 v172, s[4:7], s69 offen lds
	s_mov_b32 m0, s37
	s_nop 0
	buffer_load_dwordx4 v173, s[4:7], s69 offen lds
	s_cmp_eq_u32 s71, 12
	s_cbranch_scc1 .Lp6w0_last
	s_cmp_lg_u32 s71, -2
	s_cbranch_scc1 .Lp6w0_norm
	s_cmp_eq_u32 s99, 0
	s_cbranch_scc1 .Lp6w0_norm
	s_waitcnt vmcnt(24)
	s_branch .Lp6w0_join
.Lp6w0_last:
	s_waitcnt vmcnt(12)
	s_branch .Lp6w0_join

; #define PG8_STAGE_A(bufoff, soff, voff) do { _Pragma("unroll") for (int _i = 0; _i < 2; ++_i) \
;         __builtin_amdgcn_raw_ptr_buffer_load_lds(rsA, (LAS void*)(lds + (bufoff) + ldsw + _i * 8192), 16, (voff)[_i], (soff), 0, 0); } while (0)
; #define PG8_STAGE_B(bufoff, soff) do { _Pragma("unroll") for (int _i = 0; _i < 2; ++_i) \
;         __builtin_amdgcn_raw_ptr_buffer_load_lds(rsB, (LAS void*)(lds + (bufoff) + ldsw + _i * 8192), 16, voffB[_i], (soff), 0, 0); } while (0)
; #define PG8_LDA(dst, b, h) do { _Pragma("unroll") for (int m = 0; m < 4; ++m) dst[m] = PG8_LD8(lds + PG8_SA(b, h) + aoff + m * 2048); } while (0)
; #define PG8_WAIT_V(n) asm volatile("s_waitcnt vmcnt(" #n ")" ::: "memory")
; #define PG8_WAIT_L(n) asm volatile("s_waitcnt lgkmcnt(" #n ")" ::: "memory")
; #define PG8_BAR __builtin_amdgcn_s_barrier()
; #define PG8_SCHED __builtin_amdgcn_sched_barrier(0)
; template <class Epi, class Sched, bool GATHER, bool ALIGN_EPI, bool SP2, bool FP8>
; __device__ __forceinline__ void gemm_phase(LAS unsigned char* lds, const Gemm g, const Sched& S, const Epi& E) {
;     ...
;             PG8_WAIT_V(8); PG8_WAIT_L(0); PG8_BAR; PG8_MMA(0, 0, At, B0); PG8_MMA(0, 1, At, B1); PG8_BAR; PG8_SCHED;
;             PG8_LDA(At, 0, 1); PG8_STAGE_B(PG8_SB(0, 0), b2); PG8_STAGE_B(PG8_SB(0, 1), b2 + hstep); PG8_STAGE_A(PG8_SA(0, 0), a2, va20);
;             PG8_WAIT_V(8); PG8_WAIT_L(0); PG8_BAR; PG8_MMA(1, 0, At, B0); PG8_MMA(1, 1, At, B1); PG8_BAR; PG8_SCHED;
.Lp6w0_join:
	s_waitcnt lgkmcnt(0)
	s_barrier
	s_setprio 1
	v_mfma_f32_16x16x128_f8f6f4 v[158:161], v[2:9], v[178:185], v[158:161]
	v_mfma_f32_16x16x128_f8f6f4 v[154:157], v[10:17], v[178:185], v[154:157]
	v_mfma_f32_16x16x128_f8f6f4 v[142:145], v[2:9], v[186:193], v[142:145]
	v_mfma_f32_16x16x128_f8f6f4 v[138:141], v[10:17], v[186:193], v[138:141]
	v_mfma_f32_16x16x128_f8f6f4 v[126:129], v[2:9], v[194:201], v[126:129]
	v_mfma_f32_16x16x128_f8f6f4 v[122:125], v[10:17], v[194:201], v[122:125]
	v_mfma_f32_16x16x128_f8f6f4 v[110:113], v[2:9], v[202:209], v[110:113]
	v_mfma_f32_16x16x128_f8f6f4 v[106:109], v[10:17], v[202:209], v[106:109]
	v_mfma_f32_16x16x128_f8f6f4 v[150:153], v[210:217], v[178:185], v[150:153]
	v_mfma_f32_16x16x128_f8f6f4 v[146:149], v[218:225], v[178:185], v[146:149]
	v_mfma_f32_16x16x128_f8f6f4 v[134:137], v[210:217], v[186:193], v[134:137]
	v_mfma_f32_16x16x128_f8f6f4 v[130:133], v[218:225], v[186:193], v[130:133]
	v_mfma_f32_16x16x128_f8f6f4 v[118:121], v[210:217], v[194:201], v[118:121]
	v_mfma_f32_16x16x128_f8f6f4 v[114:117], v[218:225], v[194:201], v[114:117]
	v_mfma_f32_16x16x128_f8f6f4 v[102:105], v[210:217], v[202:209], v[102:105]
	v_mfma_f32_16x16x128_f8f6f4 v[98:101], v[218:225], v[202:209], v[98:101]
	s_setprio 0
	s_barrier
	ds_read_b128 v[178:181], v176 offset:16384
	ds_read_b128 v[182:185], v176 offset:17408
	ds_read_b128 v[186:189], v176 offset:18432
	ds_read_b128 v[190:193], v176 offset:19456
	ds_read_b128 v[194:197], v176 offset:20480
	ds_read_b128 v[198:201], v176 offset:21504
	ds_read_b128 v[202:205], v176 offset:22528
	ds_read_b128 v[206:209], v176 offset:23552
	s_mov_b32 m0, s21
	s_nop 0
	buffer_load_dwordx4 v163, s[8:11], s72 offen lds
	s_mov_b32 m0, s22
	s_nop 0
	buffer_load_dwordx4 v168, s[8:11], s72 offen lds
	s_add_i32 s75, s72, 0x40000
	s_mov_b32 m0, s24
	s_nop 0
	buffer_load_dwordx4 v163, s[8:11], s75 offen lds
	s_mov_b32 m0, s25
	s_nop 0
	buffer_load_dwordx4 v168, s[8:11], s75 offen lds
	s_mov_b32 m0, s20
	s_nop 0
	buffer_load_dwordx4 v170, s[4:7], s74 offen lds
	s_mov_b32 m0, s23
	s_nop 0
	buffer_load_dwordx4 v171, s[4:7], s74 offen lds
	s_cmp_eq_u32 s71, 12
	s_cbranch_scc1 .Lp6w1_last
	s_cmp_lg_u32 s71, -2
	s_cbranch_scc1 .Lp6w1_norm
	s_cmp_eq_u32 s99, 0
	s_cbranch_scc1 .Lp6w1_norm
	s_waitcnt vmcnt(24)
	s_branch .Lp6w1_join

; #define PG8_STAGE_A(bufoff, soff, voff) do { _Pragma("unroll") for (int _i = 0; _i < 2; ++_i) \
;         __builtin_amdgcn_raw_ptr_buffer_load_lds(rsA, (LAS void*)(lds + (bufoff) + ldsw + _i * 8192), 16, (voff)[_i], (soff), 0, 0); } while (0)
; #define PG8_STAGE_B(bufoff, soff) do { _Pragma("unroll") for (int _i = 0; _i < 2; ++_i) \
;         __builtin_amdgcn_raw_ptr_buffer_load_lds(rsB, (LAS void*)(lds + (bufoff) + ldsw + _i * 8192), 16, voffB[_i], (soff), 0, 0); } while (0)
; #define PG8_LDA(dst, b, h) do { _Pragma("unroll") for (int m = 0; m < 4; ++m) dst[m] = PG8_LD8(lds + PG8_SA(b, h) + aoff + m * 2048); } while (0)
; #define PG8_LDB(dst, b, h) do { _Pragma("unroll") for (int n = 0; n < 2; ++n) dst[n] = PG8_LD8(lds + PG8_SB(b, h) + boff + n * 2048); } while (0)
; #define PG8_WAIT_V(n) asm volatile("s_waitcnt vmcnt(" #n ")" ::: "memory")
; #define PG8_WAIT_L(n) asm volatile("s_waitcnt lgkmcnt(" #n ")" ::: "memory")
; #define PG8_BAR __builtin_amdgcn_s_barrier()
; #define PG8_SCHED __builtin_amdgcn_sched_barrier(0)
; template <class Epi, class Sched, bool GATHER, bool ALIGN_EPI, bool SP2, bool FP8>
; __device__ __forceinline__ void gemm_phase(LAS unsigned char* lds, const Gemm g, const Sched& S, const Epi& E) {
;     ...
;             PG8_WAIT_V(8); PG8_WAIT_L(0); PG8_BAR; PG8_MMA(1, 0, At, B0); PG8_MMA(1, 1, At, B1); PG8_BAR; PG8_SCHED;
;             PG8_LDB(B0, 1, 0); PG8_LDB(B1, 1, 1); PG8_SCHED; PG8_LDA(At, 1, 0); PG8_STAGE_A(PG8_SA(0, 1), a2, va21);
;             PG8_WAIT_V(8); PG8_WAIT_L(0); PG8_BAR; PG8_MMA(0, 0, At, B0); PG8_MMA(0, 1, At, B1); PG8_BAR; PG8_SCHED;
;             PG8_LDA(At, 1, 1); PG8_STAGE_B(PG8_SB(1, 0), b3); PG8_STAGE_B(PG8_SB(1, 1), b3 + hstep); PG8_STAGE_A(PG8_SA(1, 0), a3, va20);
;             PG8_WAIT_V(8); PG8_WAIT_L(0); PG8_BAR; PG8_MMA(1, 0, At, B0); PG8_MMA(1, 1, At, B1); PG8_BAR; PG8_SCHED;
.Lp6w1_join:
	s_waitcnt lgkmcnt(0)
	s_barrier
	s_setprio 1
	v_mfma_f32_16x16x128_f8f6f4 v[94:97], v[2:9], v[178:185], v[94:97]
	v_mfma_f32_16x16x128_f8f6f4 v[90:93], v[10:17], v[178:185], v[90:93]
	v_mfma_f32_16x16x128_f8f6f4 v[78:81], v[2:9], v[186:193], v[78:81]
	v_mfma_f32_16x16x128_f8f6f4 v[74:77], v[10:17], v[186:193], v[74:77]
	v_mfma_f32_16x16x128_f8f6f4 v[62:65], v[2:9], v[194:201], v[62:65]
	v_mfma_f32_16x16x128_f8f6f4 v[58:61], v[10:17], v[194:201], v[58:61]
	v_mfma_f32_16x16x128_f8f6f4 v[46:49], v[2:9], v[202:209], v[46:49]
	v_mfma_f32_16x16x128_f8f6f4 v[42:45], v[10:17], v[202:209], v[42:45]
	v_mfma_f32_16x16x128_f8f6f4 v[86:89], v[210:217], v[178:185], v[86:89]
	v_mfma_f32_16x16x128_f8f6f4 v[82:85], v[218:225], v[178:185], v[82:85]
	v_mfma_f32_16x16x128_f8f6f4 v[70:73], v[210:217], v[186:193], v[70:73]
	v_mfma_f32_16x16x128_f8f6f4 v[66:69], v[218:225], v[186:193], v[66:69]
	v_mfma_f32_16x16x128_f8f6f4 v[54:57], v[210:217], v[194:201], v[54:57]
	v_mfma_f32_16x16x128_f8f6f4 v[50:53], v[218:225], v[194:201], v[50:53]
	v_mfma_f32_16x16x128_f8f6f4 v[38:41], v[210:217], v[202:209], v[38:41]
	v_mfma_f32_16x16x128_f8f6f4 v[34:37], v[218:225], v[202:209], v[34:37]
	s_setprio 0
	s_barrier
	v_add_u32_e32 v14, 0x18000, v175
	ds_read_b128 v[2:5], v14
	ds_read_b128 v[6:9], v14 offset:1024
	ds_read_b128 v[10:13], v14 offset:2048
	ds_read_b128 v[14:17], v14 offset:3072
	v_add_u32_e32 v177, 0x1c000, v175
	ds_read_b128 v[210:213], v177
	ds_read_b128 v[214:217], v177 offset:1024
	ds_read_b128 v[218:221], v177 offset:2048
	ds_read_b128 v[222:225], v177 offset:3072
	ds_read_b128 v[178:181], v176 offset:32768
	ds_read_b128 v[182:185], v176 offset:33792
	ds_read_b128 v[186:189], v176 offset:34816
	ds_read_b128 v[190:193], v176 offset:35840
	ds_read_b128 v[194:197], v176 offset:36864
	ds_read_b128 v[198:201], v176 offset:37888
	ds_read_b128 v[202:205], v176 offset:38912
	ds_read_b128 v[206:209], v176 offset:39936
	s_mov_b32 m0, s26
	s_nop 0
	buffer_load_dwordx4 v172, s[4:7], s74 offen lds
	s_mov_b32 m0, s27
	s_nop 0
	buffer_load_dwordx4 v173, s[4:7], s74 offen lds
	s_waitcnt vmcnt(8)
	s_waitcnt lgkmcnt(0)
	s_barrier
	s_setprio 1
	v_mfma_f32_16x16x128_f8f6f4 v[158:161], v[2:9], v[178:185], v[158:161]
	v_mfma_f32_16x16x128_f8f6f4 v[154:157], v[10:17], v[178:185], v[154:157]
	v_mfma_f32_16x16x128_f8f6f4 v[142:145], v[2:9], v[186:193], v[142:145]
	v_mfma_f32_16x16x128_f8f6f4 v[138:141], v[10:17], v[186:193], v[138:141]
	v_mfma_f32_16x16x128_f8f6f4 v[126:129], v[2:9], v[194:201], v[126:129]
	v_mfma_f32_16x16x128_f8f6f4 v[122:125], v[10:17], v[194:201], v[122:125]
	v_mfma_f32_16x16x128_f8f6f4 v[110:113], v[2:9], v[202:209], v[110:113]
	v_mfma_f32_16x16x128_f8f6f4 v[106:109], v[10:17], v[202:209], v[106:109]
	v_mfma_f32_16x16x128_f8f6f4 v[150:153], v[210:217], v[178:185], v[150:153]
	v_mfma_f32_16x16x128_f8f6f4 v[146:149], v[218:225], v[178:185], v[146:149]
	v_mfma_f32_16x16x128_f8f6f4 v[134:137], v[210:217], v[186:193], v[134:137]
	v_mfma_f32_16x16x128_f8f6f4 v[130:133], v[218:225], v[186:193], v[130:133]
	v_mfma_f32_16x16x128_f8f6f4 v[118:121], v[210:217], v[194:201], v[118:121]
	v_mfma_f32_16x16x128_f8f6f4 v[114:117], v[218:225], v[194:201], v[114:117]
	v_mfma_f32_16x16x128_f8f6f4 v[102:105], v[210:217], v[202:209], v[102:105]
	v_mfma_f32_16x16x128_f8f6f4 v[98:101], v[218:225], v[202:209], v[98:101]
	s_setprio 0
	s_barrier
	ds_read_b128 v[178:181], v176 offset:49152
	ds_read_b128 v[182:185], v176 offset:50176
	ds_read_b128 v[186:189], v176 offset:51200
	ds_read_b128 v[190:193], v176 offset:52224
	ds_read_b128 v[194:197], v176 offset:53248
	ds_read_b128 v[198:201], v176 offset:54272
	ds_read_b128 v[202:205], v176 offset:55296
	ds_read_b128 v[206:209], v176 offset:56320
	s_or_b32 s72, s72, 0x80
	s_mov_b32 m0, s28
	s_nop 0
	buffer_load_dwordx4 v163, s[8:11], s72 offen lds
	s_mov_b32 m0, s29
	s_nop 0
	buffer_load_dwordx4 v168, s[8:11], s72 offen lds
	s_add_i32 s75, s72, 0x40000
	s_mov_b32 m0, s34
	s_nop 0
	buffer_load_dwordx4 v163, s[8:11], s75 offen lds
	s_mov_b32 m0, s35
	s_nop 0
	buffer_load_dwordx4 v168, s[8:11], s75 offen lds
	s_mov_b32 m0, s30
	s_nop 0
	buffer_load_dwordx4 v170, s[4:7], s73 offen lds
	s_mov_b32 m0, s31
	s_nop 0
	buffer_load_dwordx4 v171, s[4:7], s73 offen lds
	s_waitcnt vmcnt(8)
	s_waitcnt lgkmcnt(0)
	s_barrier
	s_setprio 1
	v_mfma_f32_16x16x128_f8f6f4 v[94:97], v[2:9], v[178:185], v[94:97]
	v_mfma_f32_16x16x128_f8f6f4 v[90:93], v[10:17], v[178:185], v[90:93]
	v_mfma_f32_16x16x128_f8f6f4 v[78:81], v[2:9], v[186:193], v[78:81]
	v_mfma_f32_16x16x128_f8f6f4 v[74:77], v[10:17], v[186:193], v[74:77]
	v_mfma_f32_16x16x128_f8f6f4 v[62:65], v[2:9], v[194:201], v[62:65]
	v_mfma_f32_16x16x128_f8f6f4 v[58:61], v[10:17], v[194:201], v[58:61]
	v_mfma_f32_16x16x128_f8f6f4 v[46:49], v[2:9], v[202:209], v[46:49]
	v_mfma_f32_16x16x128_f8f6f4 v[42:45], v[10:17], v[202:209], v[42:45]
	v_mfma_f32_16x16x128_f8f6f4 v[86:89], v[210:217], v[178:185], v[86:89]
	v_mfma_f32_16x16x128_f8f6f4 v[82:85], v[218:225], v[178:185], v[82:85]
	v_mfma_f32_16x16x128_f8f6f4 v[70:73], v[210:217], v[186:193], v[70:73]
	v_mfma_f32_16x16x128_f8f6f4 v[66:69], v[218:225], v[186:193], v[66:69]
	v_mfma_f32_16x16x128_f8f6f4 v[54:57], v[210:217], v[194:201], v[54:57]
	v_mfma_f32_16x16x128_f8f6f4 v[50:53], v[218:225], v[194:201], v[50:53]
	v_mfma_f32_16x16x128_f8f6f4 v[38:41], v[210:217], v[202:209], v[38:41]
	v_mfma_f32_16x16x128_f8f6f4 v[34:37], v[218:225], v[202:209], v[34:37]
	s_setprio 0
	s_add_i32 s71, s71, 2
	s_addk_i32 s69, 0x100
	s_addk_i32 s70, 0x100
	s_cmp_gt_u32 s71, 13
	s_barrier
	s_cbranch_scc1 .LBB0_1008

; #define PG8_BAR __builtin_amdgcn_s_barrier()
; template <class Epi, class Sched, bool GATHER, bool ALIGN_EPI, bool SP2, bool FP8>
; __device__ __forceinline__ void gemm_phase(LAS unsigned char* lds, const Gemm g, const Sched& S, const Epi& E) {
;     ...
;         }
;         if constexpr (ALIGN_EPI) { if (wr == 0) PG8_BAR; }
;         {
.LBB0_1008:
	s_mov_b32 s99, 1
	s_and_b64 vcc, exec, s[16:17]
	s_cbranch_vccz .LBB0_1010
	s_barrier
